# baseline (speedup 1.0000x reference)
.LBB0_26:
	s_or_b64 exec, exec, s[26:27]
	s_movk_i32 s8, 0x61a7
	s_waitcnt vmcnt(2)
	v_cmp_lt_u32_e64 s[0:1], s8, v30
	s_mov_b32 s9, 0xc34f
	s_mov_b32 s10, 0x124f7
	v_cndmask_b32_e64 v0, 0, 1, s[0:1]
	v_cmp_lt_u32_e64 s[0:1], s9, v30
	s_movk_i32 s11, 0x1f70
	s_waitcnt lgkmcnt(0)
	v_cndmask_b32_e64 v1, 0, 1, s[0:1]
	v_cmp_lt_u32_e64 s[0:1], s10, v30
	s_barrier
	s_nop 0
	v_addc_co_u32_e64 v0, s[0:1], v0, v1, s[0:1]
	v_mad_u32_u24 v1, v87, s11, v26
	v_lshlrev_b32_e32 v1, 19, v1
	v_lshl_add_u32 v0, v0, 17, v1
	v_lshlrev_b32_e32 v1, 2, v86
	v_or_b32_e32 v0, v0, v30
	ds_read_b32 v26, v84 offset:52784
	ds_read_b32 v30, v85 offset:52784
	ds_read_b32 v34, v83 offset:52784
	ds_read_b32 v35, v82 offset:52784
	ds_read_b32 v36, v81 offset:52784
	ds_read_b32 v37, v80 offset:52784
	ds_read_b32 v38, v79 offset:52784
	ds_read_b32 v39, v78 offset:52784
	s_waitcnt lgkmcnt(7)
	v_lshl_add_u32 v1, v26, 2, v1
	v_cmp_lt_u32_e64 s[0:1], s8, v31
	ds_write_b32 v1, v0
	v_cmp_lt_u32_e64 s[12:13], s9, v31
	v_cmp_lt_u32_e64 s[14:15], s10, v31
	v_cndmask_b32_e64 v0, 0, 1, s[0:1]
	v_cndmask_b32_e64 v1, 0, 1, s[12:13]
	v_addc_co_u32_e64 v0, s[14:15], v0, v1, s[14:15]
	v_mad_u32_u24 v1, v77, s11, v27
	v_lshlrev_b32_e32 v1, 19, v1
	v_lshl_add_u32 v0, v0, 17, v1
	v_lshlrev_b32_e32 v1, 2, v76
	v_or_b32_e32 v0, v0, v31
	s_waitcnt lgkmcnt(7)
	v_lshl_add_u32 v1, v30, 2, v1
	v_cmp_lt_u32_e64 s[0:1], s8, v32
	ds_write_b32 v1, v0
	v_cmp_lt_u32_e64 s[12:13], s9, v32
	v_cmp_lt_u32_e64 s[14:15], s10, v32
	v_cndmask_b32_e64 v0, 0, 1, s[0:1]
	v_cndmask_b32_e64 v1, 0, 1, s[12:13]
	v_addc_co_u32_e64 v0, s[14:15], v0, v1, s[14:15]
	v_mad_u32_u24 v1, v75, s11, v28
	v_lshlrev_b32_e32 v1, 19, v1
	v_lshl_add_u32 v0, v0, 17, v1
	v_lshlrev_b32_e32 v1, 2, v74
	v_or_b32_e32 v0, v0, v32
	s_waitcnt lgkmcnt(7)
	v_lshl_add_u32 v1, v34, 2, v1
	v_cmp_lt_u32_e64 s[0:1], s8, v33
	ds_write_b32 v1, v0
	v_cmp_lt_u32_e64 s[12:13], s9, v33
	v_cmp_lt_u32_e64 s[14:15], s10, v33
	v_cndmask_b32_e64 v0, 0, 1, s[0:1]
	v_cndmask_b32_e64 v1, 0, 1, s[12:13]
	v_addc_co_u32_e64 v0, s[14:15], v0, v1, s[14:15]
	v_mad_u32_u24 v1, v73, s11, v29
	v_lshlrev_b32_e32 v1, 19, v1
	v_lshl_add_u32 v0, v0, 17, v1
	v_lshlrev_b32_e32 v1, 2, v72
	v_or_b32_e32 v0, v0, v33
	s_waitcnt lgkmcnt(7)
	v_lshl_add_u32 v1, v35, 2, v1
	s_waitcnt vmcnt(1)
	v_cmp_lt_u32_e64 s[0:1], s8, v22
	ds_write_b32 v1, v0
	v_cmp_lt_u32_e64 s[12:13], s9, v22
	v_cmp_lt_u32_e64 s[14:15], s10, v22
	v_cndmask_b32_e64 v0, 0, 1, s[0:1]
	v_cndmask_b32_e64 v1, 0, 1, s[12:13]
	v_addc_co_u32_e64 v0, s[14:15], v0, v1, s[14:15]
	v_mad_u32_u24 v1, v71, s11, v18
	v_lshlrev_b32_e32 v1, 19, v1
	v_lshl_add_u32 v0, v0, 17, v1
	v_lshlrev_b32_e32 v1, 2, v70
	v_or_b32_e32 v0, v0, v22
	s_waitcnt lgkmcnt(7)
	v_lshl_add_u32 v1, v36, 2, v1
	v_cmp_lt_u32_e64 s[0:1], s8, v23
	ds_write_b32 v1, v0
	v_cmp_lt_u32_e64 s[12:13], s9, v23
	v_cmp_lt_u32_e64 s[14:15], s10, v23
	v_cndmask_b32_e64 v0, 0, 1, s[0:1]
	v_cndmask_b32_e64 v1, 0, 1, s[12:13]
	v_addc_co_u32_e64 v0, s[14:15], v0, v1, s[14:15]
	v_mad_u32_u24 v1, v69, s11, v19
	v_lshlrev_b32_e32 v1, 19, v1
	v_lshl_add_u32 v0, v0, 17, v1
	v_lshlrev_b32_e32 v1, 2, v68
	v_or_b32_e32 v0, v0, v23
	s_waitcnt lgkmcnt(7)
	v_lshl_add_u32 v1, v37, 2, v1
	v_cmp_lt_u32_e64 s[0:1], s8, v24
	ds_write_b32 v1, v0
	v_cmp_lt_u32_e64 s[12:13], s9, v24
	v_cmp_lt_u32_e64 s[14:15], s10, v24
	v_cndmask_b32_e64 v0, 0, 1, s[0:1]
	v_cndmask_b32_e64 v1, 0, 1, s[12:13]
	v_addc_co_u32_e64 v0, s[14:15], v0, v1, s[14:15]
	v_mad_u32_u24 v1, v67, s11, v20
	v_lshlrev_b32_e32 v1, 19, v1
	v_lshl_add_u32 v0, v0, 17, v1
	v_lshlrev_b32_e32 v1, 2, v66
	v_or_b32_e32 v0, v0, v24
	s_waitcnt lgkmcnt(7)
	v_lshl_add_u32 v1, v38, 2, v1
	v_cmp_lt_u32_e64 s[0:1], s8, v25
	ds_write_b32 v1, v0
	v_cmp_lt_u32_e64 s[12:13], s9, v25
	v_cmp_lt_u32_e64 s[14:15], s10, v25
	v_cndmask_b32_e64 v0, 0, 1, s[0:1]
	v_cndmask_b32_e64 v1, 0, 1, s[12:13]
	v_addc_co_u32_e64 v0, s[14:15], v0, v1, s[14:15]
	v_mad_u32_u24 v1, v65, s11, v21
	v_lshlrev_b32_e32 v1, 19, v1
	v_lshl_add_u32 v0, v0, 17, v1
	v_lshlrev_b32_e32 v1, 2, v63
	v_or_b32_e32 v0, v0, v25
	s_waitcnt lgkmcnt(7)
	v_lshl_add_u32 v1, v39, 2, v1
	s_waitcnt vmcnt(0)
	v_cmp_lt_u32_e64 s[0:1], s8, v14
	ds_write_b32 v1, v0
	ds_read_b32 v0, v64 offset:52784
	v_cmp_lt_u32_e64 s[12:13], s9, v14
	v_cmp_lt_u32_e64 s[14:15], s10, v14
	v_cndmask_b32_e64 v1, 0, 1, s[0:1]
	v_cndmask_b32_e64 v18, 0, 1, s[12:13]
	v_addc_co_u32_e64 v1, s[14:15], v1, v18, s[14:15]
	v_mad_u32_u24 v10, v62, s11, v10
	v_lshlrev_b32_e32 v10, 19, v10
	v_lshl_add_u32 v1, v1, 17, v10
	v_lshlrev_b32_e32 v10, 2, v60
	v_or_b32_e32 v1, v1, v14
	s_waitcnt lgkmcnt(0)
	v_lshl_add_u32 v0, v0, 2, v10
	v_cmp_lt_u32_e64 s[0:1], s8, v15
	ds_read_b32 v14, v61 offset:52784
	ds_read_b32 v18, v59 offset:52784
	ds_read_b32 v19, v58 offset:52784
	ds_write_b32 v0, v1
	v_cmp_lt_u32_e64 s[12:13], s9, v15
	v_cmp_lt_u32_e64 s[14:15], s10, v15
	v_cndmask_b32_e64 v0, 0, 1, s[0:1]
	v_cndmask_b32_e64 v1, 0, 1, s[12:13]
	v_addc_co_u32_e64 v0, s[14:15], v0, v1, s[14:15]
	v_mad_u32_u24 v1, v57, s11, v11
	v_lshlrev_b32_e32 v1, 19, v1
	v_lshl_add_u32 v0, v0, 17, v1
	v_lshlrev_b32_e32 v1, 2, v56
	v_or_b32_e32 v0, v0, v15
	s_waitcnt lgkmcnt(3)
	v_lshl_add_u32 v1, v14, 2, v1
	v_cmp_lt_u32_e64 s[0:1], s8, v16
	ds_write_b32 v1, v0
	v_cmp_lt_u32_e64 s[12:13], s9, v16
	v_cmp_lt_u32_e64 s[14:15], s10, v16
	v_cndmask_b32_e64 v0, 0, 1, s[0:1]
	v_cndmask_b32_e64 v1, 0, 1, s[12:13]
	v_addc_co_u32_e64 v0, s[14:15], v0, v1, s[14:15]
	v_mad_u32_u24 v1, v55, s11, v12
	v_lshlrev_b32_e32 v1, 19, v1
	v_lshl_add_u32 v0, v0, 17, v1
	v_lshlrev_b32_e32 v1, 2, v54
	v_or_b32_e32 v0, v0, v16
	s_waitcnt lgkmcnt(3)
	v_lshl_add_u32 v1, v18, 2, v1
	v_cmp_lt_u32_e64 s[0:1], s8, v17
	ds_write_b32 v1, v0
	v_cmp_lt_u32_e64 s[12:13], s9, v17
	v_cmp_lt_u32_e64 s[14:15], s10, v17
	v_cndmask_b32_e64 v0, 0, 1, s[0:1]
	v_cndmask_b32_e64 v1, 0, 1, s[12:13]
	v_addc_co_u32_e64 v0, s[14:15], v0, v1, s[14:15]
	v_mad_u32_u24 v1, v53, s11, v13
	v_lshlrev_b32_e32 v1, 19, v1
	v_lshl_add_u32 v0, v0, 17, v1
	v_lshlrev_b32_e32 v1, 2, v52
	v_or_b32_e32 v0, v0, v17
	s_waitcnt lgkmcnt(3)
	v_lshl_add_u32 v1, v19, 2, v1
	ds_write_b32 v1, v0
	s_and_saveexec_b64 s[2:3], s[4:5]
	s_cbranch_execz .LBB0_28
	s_mov_b32 s4, 0x38e38e39
	v_mul_hi_u32 v0, v2, s4
	v_lshrrev_b32_e32 v0, 5, v0
	v_cmp_lt_u32_e64 s[0:1], s8, v6
	v_lshlrev_b32_e32 v1, 2, v0
	ds_read_b32 v1, v1 offset:52784
	v_cndmask_b32_e64 v10, 0, 1, s[0:1]
	v_cmp_lt_u32_e64 s[0:1], s9, v6
	v_mad_u32_u24 v0, v0, s11, v2
	v_lshlrev_b32_e32 v0, 19, v0
	v_cndmask_b32_e64 v11, 0, 1, s[0:1]
	v_cmp_lt_u32_e64 s[0:1], s10, v6
	v_mul_hi_u32 v13, v5, s4
	v_lshlrev_b32_e32 v2, 2, v51
	v_addc_co_u32_e64 v10, s[0:1], v10, v11, s[0:1]
	v_lshl_add_u32 v0, v10, 17, v0
	v_or_b32_e32 v0, v0, v6
	v_mul_hi_u32 v6, v3, s4
	v_mul_hi_u32 v11, v4, s4
	v_lshrrev_b32_e32 v6, 5, v6
	v_lshrrev_b32_e32 v11, 5, v11
	v_lshrrev_b32_e32 v13, 5, v13
	v_lshlrev_b32_e32 v10, 2, v6
	v_lshlrev_b32_e32 v12, 2, v11
	v_lshlrev_b32_e32 v14, 2, v13
	s_waitcnt lgkmcnt(0)
	v_lshl_add_u32 v1, v1, 2, v2
	v_cmp_lt_u32_e64 s[0:1], s8, v7
	ds_read_b32 v10, v10 offset:52784
	ds_read_b32 v12, v12 offset:52784
	ds_read_b32 v14, v14 offset:52784
	ds_write_b32 v1, v0
	v_cmp_lt_u32_e64 s[12:13], s9, v7
	v_cmp_lt_u32_e64 s[14:15], s10, v7
	v_cndmask_b32_e64 v0, 0, 1, s[0:1]
	v_cndmask_b32_e64 v1, 0, 1, s[12:13]
	v_addc_co_u32_e64 v0, s[14:15], v0, v1, s[14:15]
	v_mad_u32_u24 v1, v6, s11, v3
	v_lshlrev_b32_e32 v1, 19, v1
	v_lshl_add_u32 v0, v0, 17, v1
	v_lshlrev_b32_e32 v1, 2, v50
	v_or_b32_e32 v0, v0, v7
	s_waitcnt lgkmcnt(3)
	v_lshl_add_u32 v1, v10, 2, v1
	v_cmp_lt_u32_e64 s[0:1], s8, v8
	ds_write_b32 v1, v0
	v_cmp_lt_u32_e64 s[12:13], s9, v8
	v_cmp_lt_u32_e64 s[14:15], s10, v8
	v_cndmask_b32_e64 v0, 0, 1, s[0:1]
	v_cndmask_b32_e64 v1, 0, 1, s[12:13]
	v_addc_co_u32_e64 v0, s[14:15], v0, v1, s[14:15]
	v_mad_u32_u24 v1, v11, s11, v4
	v_lshlrev_b32_e32 v1, 19, v1
	v_lshl_add_u32 v0, v0, 17, v1
	v_lshlrev_b32_e32 v1, 2, v49
	v_or_b32_e32 v0, v0, v8
	s_waitcnt lgkmcnt(3)
	v_lshl_add_u32 v1, v12, 2, v1
	v_cmp_lt_u32_e64 s[0:1], s8, v9
	ds_write_b32 v1, v0
	v_cmp_lt_u32_e64 s[12:13], s9, v9
	v_cmp_lt_u32_e64 s[14:15], s10, v9
	v_cndmask_b32_e64 v0, 0, 1, s[0:1]
	v_cndmask_b32_e64 v1, 0, 1, s[12:13]
	v_addc_co_u32_e64 v0, s[14:15], v0, v1, s[14:15]
	v_mad_u32_u24 v1, v13, s11, v5
	v_lshlrev_b32_e32 v1, 19, v1
	v_lshl_add_u32 v0, v0, 17, v1
	v_lshlrev_b32_e32 v1, 2, v48
	v_or_b32_e32 v0, v0, v9
	s_waitcnt lgkmcnt(3)
	v_lshl_add_u32 v1, v14, 2, v1
	ds_write_b32 v1, v0
